# P6 epilogue: X1 rows of the sweep's later tokens touched early (cold lines pulled into L2 while the first token's epilogue runs)
# speedup vs baseline: 1.0455x; 1.0061x over previous
.LBB0_975:
	s_add_i32 s0, s96, s35
	s_ashr_i32 s1, s0, 31
	s_lshr_b32 s1, s1, 19
	s_add_i32 s0, s0, s1
	s_ashr_i32 s2, s0, 13
	s_xor_b64 s[14:15], s[6:7], -1
	s_ashr_i32 s0, s2, 31
	s_add_u32 s1, s2, s87
	s_addc_u32 s0, s0, 0
	s_waitcnt vmcnt(0)
	v_readlane_b32 s40, v253, 62
	v_readlane_b32 s41, v253, 63
	s_lshl_b64 s[44:45], s[96:97], 12
	v_lshlrev_b32_e32 v2, 6, v179
	s_add_u32 s40, s40, s44
	s_addc_u32 s41, s41, s45
	s_add_u32 s40, s40, 0x1000
	s_addc_u32 s41, s41, 0
	global_load_dword v4, v2, s[40:41]
	s_add_u32 s40, s40, 0x1000
	s_addc_u32 s41, s41, 0
	global_load_dword v4, v2, s[40:41]
	s_add_u32 s40, s40, 0x1000
	s_addc_u32 s41, s41, 0
	global_load_dword v4, v2, s[40:41]
	v_mov_b32_e32 v1, v179
	s_mulk_i32 s0, 0x6000
	s_mul_hi_u32 s3, s1, 0x6000
	s_add_i32 s3, s3, s0
	s_mulk_i32 s1, 0x6000
	v_lshlrev_b32_e32 v20, 4, v1
	s_add_u32 s6, s70, s1
	v_readlane_b32 s36, v253, 60
	v_ashrrev_i32_e32 v21, 31, v20
	s_addc_u32 s7, s71, s3
	s_lshl_b64 s[0:1], s[96:97], 12
	v_readlane_b32 s38, v253, 62
	v_lshlrev_b64 v[22:23], 2, v[20:21]
	v_readlane_b32 s39, v253, 63
	s_add_u32 s20, s38, s0
	v_lshl_add_u64 v[68:69], s[6:7], 0, v[22:23]
	s_mov_b64 s[6:7], 0x5000
	s_addc_u32 s21, s39, s1
	v_lshl_add_u64 v[12:13], v[68:69], 0, s[6:7]
	s_lshl_b64 s[6:7], s[96:97], 3
	v_lshl_add_u64 v[32:33], s[20:21], 0, v[22:23]
	s_add_u32 s6, s64, s6
	global_load_dwordx4 v[4:7], v[12:13], off offset:48
	global_load_dwordx4 v[8:11], v[12:13], off offset:32
	s_addc_u32 s7, s65, s7
	global_load_dwordx4 v[12:15], v[12:13], off offset:16
	s_nop 0
	global_load_dwordx2 v[72:73], v3, s[6:7]
	global_load_dwordx4 v[16:19], v[32:33], off
	global_load_dwordx4 v[24:27], v[32:33], off offset:16
	global_load_dwordx4 v[28:31], v[32:33], off offset:32
	s_nop 0
	global_load_dwordx4 v[32:35], v[32:33], off offset:48
	v_lshl_add_u64 v[60:61], s[16:17], 0, v[22:23]
	v_lshl_add_u64 v[64:65], s[28:29], 0, v[22:23]
	v_add_co_u32_e32 v68, vcc, s18, v68
	global_load_dwordx4 v[36:39], v[64:65], off offset:48
	global_load_dwordx4 v[40:43], v[60:61], off offset:48
	global_load_dwordx4 v[44:47], v[60:61], off offset:32
	global_load_dwordx4 v[48:51], v[64:65], off offset:32
	global_load_dwordx4 v[52:55], v[64:65], off offset:16
	global_load_dwordx4 v[56:59], v[60:61], off offset:16
	s_nop 0
	global_load_dwordx4 v[60:63], v[60:61], off
	s_nop 0
	global_load_dwordx4 v[64:67], v[64:65], off
	v_addc_co_u32_e32 v69, vcc, 0, v69, vcc
	global_load_dwordx4 v[68:71], v[68:69], off
	v_add_u32_e32 v142, 64, v183
	v_xor_b32_e32 v1, 1, v178
	v_xor_b32_e32 v2, 2, v178
	v_cmp_lt_i32_e32 vcc, v1, v142
	v_xor_b32_e32 v74, 4, v178
	v_readlane_b32 s20, v255, 42
	v_cndmask_b32_e32 v1, v178, v1, vcc
	v_cmp_lt_i32_e32 vcc, v2, v142
	v_readlane_b32 s22, v255, 44
	s_add_u32 s0, s30, s0
	v_cndmask_b32_e32 v75, v178, v2, vcc
	v_lshlrev_b32_e32 v2, 2, v1
	v_lshlrev_b32_e32 v1, 2, v75
	v_cmp_lt_i32_e32 vcc, v74, v142
	s_addc_u32 s1, s31, s1
	v_readlane_b32 s37, v253, 61
	v_readlane_b32 s40, v254, 0
	v_readlane_b32 s41, v254, 1
	v_readlane_b32 s42, v254, 2
	v_readlane_b32 s43, v254, 3
	v_readlane_b32 s44, v254, 4
	v_readlane_b32 s45, v254, 5
	v_readlane_b32 s46, v254, 6
	v_readlane_b32 s47, v254, 7
	v_readlane_b32 s48, v254, 8
	v_readlane_b32 s49, v254, 9
	v_readlane_b32 s50, v254, 10
	v_readlane_b32 s51, v254, 11
	v_readlane_b32 s21, v255, 43
	v_readlane_b32 s23, v255, 45
	s_waitcnt vmcnt(14)
	v_pk_add_f32 v[12:13], v[12:13], 1.0 op_sel_hi:[1,0]
	v_pk_add_f32 v[14:15], v[14:15], 1.0 op_sel_hi:[1,0]
	s_waitcnt vmcnt(12)
	v_pk_add_f32 v[18:19], v[18:19], v[72:73] op_sel_hi:[1,0] neg_lo:[0,1] neg_hi:[0,1]
	v_pk_add_f32 v[4:5], v[4:5], 1.0 op_sel_hi:[1,0]
	v_pk_mul_f32 v[18:19], v[72:73], v[18:19] op_sel:[1,0]
	s_waitcnt vmcnt(9)
	v_pk_add_f32 v[32:33], v[32:33], v[72:73] op_sel_hi:[1,0] neg_lo:[0,1] neg_hi:[0,1]
	v_pk_add_f32 v[34:35], v[34:35], v[72:73] op_sel_hi:[1,0] neg_lo:[0,1] neg_hi:[0,1]
	v_pk_mul_f32 v[32:33], v[72:73], v[32:33] op_sel:[1,0]
	v_pk_mul_f32 v[34:35], v[72:73], v[34:35] op_sel:[1,0]
	s_waitcnt vmcnt(7)
	v_pk_fma_f32 v[32:33], v[32:33], v[40:41], v[36:37]
	v_pk_fma_f32 v[34:35], v[34:35], v[42:43], v[38:39]
	v_pk_mul_f32 v[32:33], v[32:33], s[34:35] op_sel_hi:[1,0]
	v_pk_add_f32 v[6:7], v[6:7], 1.0 op_sel_hi:[1,0]
	v_pk_add_f32 v[24:25], v[24:25], v[72:73] op_sel_hi:[1,0] neg_lo:[0,1] neg_hi:[0,1]
	v_pk_mul_f32 v[34:35], v[34:35], s[34:35] op_sel_hi:[1,0]
	v_pk_fma_f32 v[42:43], v[138:139], v[4:5], v[32:33]
	s_waitcnt vmcnt(1)
	v_pk_fma_f32 v[4:5], v[18:19], v[62:63], v[66:67]
	v_pk_add_f32 v[16:17], v[16:17], v[72:73] op_sel_hi:[1,0] neg_lo:[0,1] neg_hi:[0,1]
	v_pk_mul_f32 v[24:25], v[72:73], v[24:25] op_sel:[1,0]
	v_pk_fma_f32 v[40:41], v[140:141], v[6:7], v[34:35]
	v_pk_mul_f32 v[4:5], v[4:5], s[34:35] op_sel_hi:[1,0]
	s_waitcnt vmcnt(0)
	v_pk_add_f32 v[6:7], v[70:71], 1.0 op_sel_hi:[1,0]
	v_pk_fma_f32 v[24:25], v[24:25], v[56:57], v[52:53]
	v_pk_fma_f32 v[52:53], v[128:129], v[6:7], v[4:5]
	v_pk_mul_f32 v[4:5], v[72:73], v[16:17] op_sel:[1,0]
	v_pk_add_f32 v[26:27], v[26:27], v[72:73] op_sel_hi:[1,0] neg_lo:[0,1] neg_hi:[0,1]
	v_pk_fma_f32 v[4:5], v[60:61], v[4:5], v[64:65]
	v_pk_mul_f32 v[26:27], v[72:73], v[26:27] op_sel:[1,0]
	v_pk_mul_f32 v[4:5], v[4:5], s[34:35] op_sel_hi:[1,0]
	v_pk_add_f32 v[6:7], v[68:69], 1.0 op_sel_hi:[1,0]
	v_pk_fma_f32 v[26:27], v[26:27], v[58:59], v[54:55]
	v_pk_fma_f32 v[54:55], v[126:127], v[6:7], v[4:5]
	v_pk_add_f32 v[30:31], v[30:31], v[72:73] op_sel_hi:[1,0] neg_lo:[0,1] neg_hi:[0,1]
	v_add_f32_e32 v4, 0, v54
	v_add_f32_e32 v4, v4, v55
	v_pk_mul_f32 v[30:31], v[72:73], v[30:31] op_sel:[1,0]
	v_pk_mul_f32 v[24:25], v[24:25], s[34:35] op_sel_hi:[1,0]
	v_add_f32_e32 v4, v4, v52
	v_pk_add_f32 v[28:29], v[28:29], v[72:73] op_sel_hi:[1,0] neg_lo:[0,1] neg_hi:[0,1]
	v_pk_fma_f32 v[30:31], v[30:31], v[46:47], v[50:51]
	v_pk_fma_f32 v[50:51], v[130:131], v[12:13], v[24:25]
	v_add_f32_e32 v4, v4, v53
	v_pk_mul_f32 v[28:29], v[72:73], v[28:29] op_sel:[1,0]
	v_pk_mul_f32 v[26:27], v[26:27], s[34:35] op_sel_hi:[1,0]
	v_add_f32_e32 v4, v4, v50
	v_pk_fma_f32 v[28:29], v[28:29], v[44:45], v[48:49]
	v_pk_fma_f32 v[48:49], v[132:133], v[14:15], v[26:27]
	v_add_f32_e32 v4, v4, v51
	v_pk_add_f32 v[8:9], v[8:9], 1.0 op_sel_hi:[1,0]
	v_pk_mul_f32 v[28:29], v[28:29], s[34:35] op_sel_hi:[1,0]
	v_add_f32_e32 v4, v4, v48
	v_pk_fma_f32 v[46:47], v[134:135], v[8:9], v[28:29]
	v_add_f32_e32 v4, v4, v49
	v_pk_add_f32 v[10:11], v[10:11], 1.0 op_sel_hi:[1,0]
	v_pk_mul_f32 v[30:31], v[30:31], s[34:35] op_sel_hi:[1,0]
	v_add_f32_e32 v4, v4, v46
	v_pk_fma_f32 v[44:45], v[136:137], v[10:11], v[30:31]
	v_add_f32_e32 v4, v4, v47
	v_add_f32_e32 v4, v4, v44
	v_add_f32_e32 v4, v4, v45
	v_add_f32_e32 v4, v4, v42
	v_add_f32_e32 v4, v4, v43
	v_add_f32_e32 v4, v4, v40
	v_add_f32_e32 v4, v4, v41
	ds_bpermute_b32 v5, v2, v4
	v_cndmask_b32_e32 v6, v178, v74, vcc
	v_lshlrev_b32_e32 v74, 2, v6
	v_xor_b32_e32 v6, 8, v178
	v_cmp_lt_i32_e32 vcc, v6, v142
	s_waitcnt lgkmcnt(0)
	v_add_f32_e32 v4, v4, v5
	ds_bpermute_b32 v5, v1, v4
	v_cndmask_b32_e32 v6, v178, v6, vcc
	v_lshlrev_b32_e32 v75, 2, v6
	v_xor_b32_e32 v6, 16, v178
	v_cmp_lt_i32_e32 vcc, v6, v142
	s_waitcnt lgkmcnt(0)
	v_add_f32_e32 v4, v4, v5
	ds_bpermute_b32 v5, v74, v4
	v_cndmask_b32_e32 v6, v178, v6, vcc
	v_lshlrev_b32_e32 v126, 2, v6
	v_xor_b32_e32 v6, 32, v178
	v_cmp_lt_i32_e32 vcc, v6, v142
	s_waitcnt lgkmcnt(0)
	v_add_f32_e32 v7, v4, v5
	ds_bpermute_b32 v8, v75, v7
	v_cndmask_b32_e32 v4, v178, v6, vcc
	v_lshlrev_b32_e32 v127, 2, v4
	v_lshl_add_u64 v[4:5], s[12:13], 0, v[22:23]
	v_lshl_add_u64 v[36:37], s[90:91], 0, v[22:23]
	s_waitcnt lgkmcnt(0)
	v_add_f32_e32 v24, v7, v8
	ds_bpermute_b32 v25, v126, v24
	global_load_dwordx4 v[16:19], v[4:5], off offset:48
	global_load_dwordx4 v[12:15], v[4:5], off offset:32
	global_load_dwordx4 v[8:11], v[4:5], off offset:16
	s_nop 0
	global_load_dwordx4 v[4:7], v[4:5], off
	v_lshl_add_u64 v[22:23], s[0:1], 0, v[22:23]
	v_readlane_b32 s0, v255, 23
	v_readlane_b32 s1, v255, 24
	s_waitcnt lgkmcnt(0)
	v_add_f32_e32 v56, v24, v25
	global_load_dwordx4 v[24:27], v[36:37], off offset:48
	global_load_dwordx4 v[28:31], v[36:37], off offset:32
	global_load_dwordx4 v[32:35], v[36:37], off offset:16
	s_nop 0
	global_load_dwordx4 v[36:39], v[36:37], off
	ds_bpermute_b32 v57, v127, v56
	s_waitcnt lgkmcnt(0)
	v_add_f32_e32 v56, v56, v57
	v_mul_f32_e32 v56, 0x3a800000, v56
	v_pk_add_f32 v[54:55], v[54:55], v[56:57] op_sel_hi:[1,0] neg_lo:[0,1] neg_hi:[0,1]
	v_pk_add_f32 v[52:53], v[52:53], v[56:57] op_sel_hi:[1,0] neg_lo:[0,1] neg_hi:[0,1]
	v_pk_mul_f32 v[58:59], v[54:55], v[54:55]
	v_pk_mul_f32 v[60:61], v[52:53], v[52:53]
	v_add_f32_e32 v58, v58, v59
	v_pk_add_f32 v[50:51], v[50:51], v[56:57] op_sel_hi:[1,0] neg_lo:[0,1] neg_hi:[0,1]
	v_add_f32_e32 v58, v60, v58
	v_pk_mul_f32 v[62:63], v[50:51], v[50:51]
	v_add_f32_e32 v58, v61, v58
	v_pk_add_f32 v[48:49], v[48:49], v[56:57] op_sel_hi:[1,0] neg_lo:[0,1] neg_hi:[0,1]
	v_add_f32_e32 v58, v62, v58
	v_pk_mul_f32 v[64:65], v[48:49], v[48:49]
	v_add_f32_e32 v58, v63, v58
	v_pk_add_f32 v[46:47], v[46:47], v[56:57] op_sel_hi:[1,0] neg_lo:[0,1] neg_hi:[0,1]
	v_add_f32_e32 v58, v64, v58
	v_pk_mul_f32 v[66:67], v[46:47], v[46:47]
	v_add_f32_e32 v58, v65, v58
	v_pk_add_f32 v[44:45], v[44:45], v[56:57] op_sel_hi:[1,0] neg_lo:[0,1] neg_hi:[0,1]
	v_add_f32_e32 v58, v66, v58
	v_pk_mul_f32 v[68:69], v[44:45], v[44:45]
	v_add_f32_e32 v58, v67, v58
	v_pk_add_f32 v[42:43], v[42:43], v[56:57] op_sel_hi:[1,0] neg_lo:[0,1] neg_hi:[0,1]
	v_add_f32_e32 v58, v68, v58
	v_pk_mul_f32 v[70:71], v[42:43], v[42:43]
	v_add_f32_e32 v58, v69, v58
	v_pk_add_f32 v[40:41], v[40:41], v[56:57] op_sel_hi:[1,0] neg_lo:[0,1] neg_hi:[0,1]
	v_add_f32_e32 v58, v70, v58
	v_pk_mul_f32 v[56:57], v[40:41], v[40:41]
	v_add_f32_e32 v58, v71, v58
	v_add_f32_e32 v56, v56, v58
	v_add_f32_e32 v56, v57, v56
	ds_bpermute_b32 v57, v2, v56
	s_waitcnt lgkmcnt(0)
	v_add_f32_e32 v56, v56, v57
	ds_bpermute_b32 v57, v1, v56
	s_waitcnt lgkmcnt(0)
	v_add_f32_e32 v56, v56, v57
	ds_bpermute_b32 v57, v74, v56
	s_waitcnt lgkmcnt(0)
	v_add_f32_e32 v56, v56, v57
	ds_bpermute_b32 v57, v75, v56
	s_waitcnt lgkmcnt(0)
	v_add_f32_e32 v56, v56, v57
	ds_bpermute_b32 v57, v126, v56
	s_waitcnt lgkmcnt(0)
	v_add_f32_e32 v56, v56, v57
	ds_bpermute_b32 v57, v127, v56
	s_waitcnt lgkmcnt(0)
	v_add_f32_e32 v56, v56, v57
	v_fmamk_f32 v56, v56, 0x3a800000, v204
	v_mul_f32_e32 v57, 0x4b800000, v56
	v_cmp_gt_f32_e32 vcc, s22, v56
	s_nop 1
	v_cndmask_b32_e32 v56, v56, v57, vcc
	v_rsq_f32_e32 v56, v56
	s_nop 0
	v_mul_f32_e32 v57, 0x45800000, v56
	v_cndmask_b32_e32 v56, v56, v57, vcc
	v_pk_mul_f32 v[54:55], v[54:55], v[56:57] op_sel_hi:[1,0]
	v_pk_mul_f32 v[52:53], v[52:53], v[56:57] op_sel_hi:[1,0]
	s_waitcnt vmcnt(0)
	v_pk_fma_f32 v[4:5], v[4:5], v[54:55], v[36:37]
	v_pk_mul_f32 v[36:37], v[50:51], v[56:57] op_sel_hi:[1,0]
	v_pk_fma_f32 v[6:7], v[6:7], v[52:53], v[38:39]
	v_pk_fma_f32 v[8:9], v[8:9], v[36:37], v[32:33]
	v_pk_mul_f32 v[32:33], v[48:49], v[56:57] op_sel_hi:[1,0]
	s_and_b64 vcc, exec, s[0:1]
	v_pk_fma_f32 v[10:11], v[10:11], v[32:33], v[34:35]
	v_pk_mul_f32 v[32:33], v[46:47], v[56:57] op_sel_hi:[1,0]
	s_nop 0
	v_pk_fma_f32 v[12:13], v[12:13], v[32:33], v[28:29]
	v_pk_mul_f32 v[28:29], v[44:45], v[56:57] op_sel_hi:[1,0]
	s_nop 0
	v_pk_fma_f32 v[14:15], v[14:15], v[28:29], v[30:31]
	v_pk_mul_f32 v[28:29], v[42:43], v[56:57] op_sel_hi:[1,0]
	s_nop 0
	v_pk_fma_f32 v[16:17], v[16:17], v[28:29], v[24:25]
	v_pk_mul_f32 v[24:25], v[40:41], v[56:57] op_sel_hi:[1,0]
	s_nop 0
	v_pk_fma_f32 v[18:19], v[18:19], v[24:25], v[26:27]
	global_store_dwordx4 v[22:23], v[4:7], off
	global_store_dwordx4 v[22:23], v[8:11], off offset:16
	global_store_dwordx4 v[22:23], v[12:15], off offset:32
	global_store_dwordx4 v[22:23], v[16:19], off offset:48
	s_cbranch_vccz .LBB0_977
	s_lshl_b64 s[0:1], s[96:97], 10
	s_mul_hi_i32 s3, s2, 0x6000
	s_mulk_i32 s2, 0x6000
	s_add_u32 s2, s70, s2
	s_addc_u32 s3, s71, s3
	v_lshl_add_u64 v[50:51], v[20:21], 2, s[2:3]
	s_mov_b64 s[2:3], 0x19000
	v_add_co_u32_e32 v34, vcc, s86, v50
	v_lshl_add_u64 v[30:31], v[50:51], 0, s[2:3]
	s_mov_b64 s[2:3], 0x18000
	v_addc_co_u32_e32 v35, vcc, 0, v51, vcc
	v_lshl_add_u64 v[46:47], v[50:51], 0, s[2:3]
	v_add_co_u32_e32 v50, vcc, s67, v50
	global_load_dwordx4 v[22:25], v[30:31], off offset:32
	global_load_dwordx4 v[26:29], v[30:31], off offset:16
	v_addc_co_u32_e32 v51, vcc, 0, v51, vcc
	global_load_dwordx4 v[30:33], v[30:31], off offset:48
	s_nop 0
	global_load_dwordx4 v[34:37], v[34:35], off
	s_nop 0
	global_load_dwordx4 v[38:41], v[46:47], off offset:16
	global_load_dwordx4 v[42:45], v[46:47], off offset:48
	s_nop 0
	global_load_dwordx4 v[46:49], v[46:47], off offset:32
	s_lshl_b64 s[0:1], s[0:1], 1
	global_load_dwordx4 v[50:53], v[50:51], off
	s_add_u32 s0, s76, s0
	s_addc_u32 s1, s77, s1
	v_lshl_add_u64 v[20:21], v[20:21], 1, s[0:1]
	s_waitcnt vmcnt(7)
	v_pk_add_f32 v[22:23], v[22:23], 1.0 op_sel_hi:[1,0]
	s_waitcnt vmcnt(6)
	v_pk_add_f32 v[26:27], v[26:27], 1.0 op_sel_hi:[1,0]
	v_pk_add_f32 v[28:29], v[28:29], 1.0 op_sel_hi:[1,0]
	s_waitcnt vmcnt(4)
	v_pk_add_f32 v[34:35], v[34:35], 1.0 op_sel_hi:[1,0]
	v_pk_add_f32 v[36:37], v[36:37], 1.0 op_sel_hi:[1,0]
	v_pk_add_f32 v[24:25], v[24:25], 1.0 op_sel_hi:[1,0]
	v_pk_add_f32 v[30:31], v[30:31], 1.0 op_sel_hi:[1,0]
	v_pk_add_f32 v[32:33], v[32:33], 1.0 op_sel_hi:[1,0]
	s_waitcnt vmcnt(3)
	v_pk_fma_f32 v[8:9], v[8:9], v[26:27], v[38:39]
	v_pk_fma_f32 v[10:11], v[10:11], v[28:29], v[40:41]
	s_waitcnt vmcnt(1)
	v_pk_fma_f32 v[12:13], v[12:13], v[22:23], v[46:47]
	s_waitcnt vmcnt(0)
	v_pk_fma_f32 v[4:5], v[4:5], v[34:35], v[50:51]
	v_pk_fma_f32 v[22:23], v[6:7], v[36:37], v[52:53]
	v_pk_fma_f32 v[14:15], v[14:15], v[24:25], v[48:49]
	v_pk_fma_f32 v[16:17], v[16:17], v[30:31], v[42:43]
	v_pk_fma_f32 v[18:19], v[18:19], v[32:33], v[44:45]
	v_cvt_pk_bf16_f32 v6, v8, v9
	v_cvt_pk_bf16_f32 v7, v10, v11
	v_cvt_pk_bf16_f32 v4, v4, v5
	v_cvt_pk_bf16_f32 v5, v22, v23
	v_cvt_pk_bf16_f32 v8, v12, v13
	v_cvt_pk_bf16_f32 v9, v14, v15
	v_cvt_pk_bf16_f32 v10, v16, v17
	v_cvt_pk_bf16_f32 v11, v18, v19
	global_store_dwordx4 v[20:21], v[4:7], off
	global_store_dwordx4 v[20:21], v[8:11], off offset:16
